# stage 1b: the inverse wave's SIMD partner takes no tiles, six waves take eight tiles each
# baseline (speedup 1.0000x reference)
.LBB0_378:
	s_cmpk_gt_i32 s18, 0x10ff
	s_cbranch_scc1 .LBB0_450
	s_movk_i32 s0, 0x280
	v_cmp_gt_i32_e64 s[0:1], s0, v92
	s_mov_b32 s10, s27
	v_add_u32_e32 v113, 0x12000, v111
	v_writelane_b32 v255, s0, 6
	s_movk_i32 s6, 0x2400
	v_add_u32_e32 v114, 0x1d400, v111
	v_writelane_b32 v255, s1, 7
	v_readlane_b32 s76, v253, 26
	v_readlane_b32 s8, v255, 4
	v_readlane_b32 s9, v255, 5
	s_add_u32 s0, s8, 0x39c00000
	s_addc_u32 s1, s9, 0
	s_add_u32 s51, s8, 0xa700000
	s_addc_u32 s70, s9, 0
	v_writelane_b32 v255, s0, 8
	s_add_u32 s71, s8, 0xa800000
	s_addc_u32 s49, s9, 0
	v_writelane_b32 v255, s1, 9
	s_ashr_i32 s0, s15, 1
	s_lshl_b32 s62, s0, 4
	s_and_b32 s27, s62, 0xffffffe0
	s_or_b32 s63, s62, 16
	s_add_u32 s2, s8, 0x48a00000
	s_addc_u32 s3, s9, 0
	s_lshl_b32 s1, s15, 5
	s_and_b32 s64, s1, 32
	s_lshl_b32 s1, s0, 5
	s_cmp_lg_u32 s15, 0
	v_writelane_b32 v255, s2, 10
	s_cselect_b64 s[54:55], -1, 0
	s_cmp_lt_i32 s15, 49
	v_writelane_b32 v255, s3, 11
	s_cselect_b64 s[2:3], -1, 0
	s_lshl_b32 s4, s15, 1
	s_and_b32 s4, s4, 2
	v_add_u32_e32 v129, s1, v113
	v_add_u32_e32 v130, s1, v111
	s_or_b32 s1, s4, 1
	s_lshl_b32 s65, s4, 4
	s_lshl_b32 s66, s1, 4
	s_and_b32 s5, s15, 3
	s_cmp_gt_i32 s15, 3
	v_writelane_b32 v255, s2, 12
	s_cselect_b64 s[68:69], -1, 0
	s_cmp_lt_i32 s15, 4
	v_writelane_b32 v255, s3, 13
	s_cselect_b32 s6, s6, 0x6c00
	s_lshl_b32 s67, s5, 4
	s_lshl_b32 s2, s5, 5
	s_lshl_b32 s5, s0, 2
	s_and_b32 s3, s15, 0x1ffffffc
	s_and_b32 s16, s5, 4
	s_add_u32 s17, s8, 0x3be00000
	s_addc_u32 s44, s9, 0
	s_add_u32 s45, s8, 0x3e000000
	s_addc_u32 s58, s9, 0
	s_add_u32 s59, s8, 0x40200000
	s_addc_u32 s35, s9, 0
	s_add_u32 s56, s8, 0x42400000
	v_add_u32_e32 v132, s6, v111
	v_lshl_add_u32 v133, s0, 6, v114
	s_addc_u32 s92, s9, 0
	s_lshl_b32 s95, s0, 10
	s_lshl_b32 s97, s0, 8
	s_lshl_b32 s50, s1, 8
	s_lshl_b32 s6, s1, 10
	v_readlane_b32 s0, v255, 1
	v_readlane_b32 s80, v253, 30
	v_readlane_b32 s81, v253, 31
	v_readlane_b32 s82, v253, 32
	v_readlane_b32 s83, v253, 33
	v_readlane_b32 s84, v253, 34
	v_readlane_b32 s85, v253, 35
	v_readlane_b32 s86, v253, 36
	v_readlane_b32 s87, v253, 37
	v_readlane_b32 s1, v255, 2
	s_mul_i32 s28, s0, 0x1b40
	v_readlane_b32 s88, v253, 38
	v_readlane_b32 s89, v253, 39
	v_readlane_b32 s90, v253, 40
	v_readlane_b32 s91, v253, 41
	s_mov_b64 s[80:81], s[84:85]
	s_lshl_b32 s93, s4, 8
	s_lshl_b32 s96, s4, 10
	s_mov_b32 s8, s0
	s_lshl_b64 s[0:1], s[28:29], 2
	s_mov_b64 s[82:83], s[86:87]
	s_mov_b64 s[84:85], s[88:89]
	v_readlane_b32 s77, v253, 27
	v_readlane_b32 s78, v253, 28
	v_readlane_b32 s79, v253, 29
	s_mov_b64 s[86:87], s[90:91]
	s_add_u32 s14, s84, s0
	s_mov_b32 s9, s15
	s_addc_u32 s15, s85, s1
	v_readlane_b32 s72, v253, 42
	s_lshl_b32 s28, s8, 10
	v_readlane_b32 s80, v253, 50
	s_lshl_b64 s[0:1], s[28:29], 2
	v_readlane_b32 s81, v253, 51
	s_add_u32 s7, s80, s0
	v_readlane_b32 s82, v253, 52
	s_addc_u32 s4, s81, s1
	s_lshl_b32 s5, s8, 11
	v_max_i32_e32 v1, 0x80, v92
	v_readlane_b32 s83, v253, 53
	s_add_u32 s42, s82, s0
	v_sub_u32_e32 v1, v1, v92
	v_readlane_b32 s84, v253, 54
	s_addc_u32 s36, s83, s1
	v_add_u32_e32 v1, 0x1ff, v1
	v_readlane_b32 s85, v253, 55
	s_add_u32 s52, s84, s0
	v_lshrrev_b32_e32 v2, 9, v1
	s_movk_i32 s0, 0x1ff
	s_addc_u32 s53, s85, s1
	v_add_u32_e32 v2, 1, v2
	v_cmp_lt_u32_e64 s[0:1], s0, v1
	v_and_b32_e32 v134, 0xfffffe, v2
	v_add_u32_e32 v118, 0x1f100, v111
	v_writelane_b32 v255, s0, 14
	v_lshlrev_b32_e32 v1, 2, v26
	v_readlane_b32 s75, v253, 45
	v_writelane_b32 v255, s1, 15
	v_cmp_ne_u32_e64 s[0:1], v2, v134
	v_and_b32_e32 v0, 63, v26
	v_add_u32_e32 v112, 0x1e900, v111
	v_writelane_b32 v255, s0, 16
	v_add_u32_e32 v115, 0x1eb00, v111
	v_add_u32_e32 v116, 0x1ed00, v111
	v_writelane_b32 v255, s1, 17
	s_lshl_b32 s0, s9, 8
	v_add3_u32 v136, s0, v1, v118
	s_add_i32 s0, s9, -8
	v_writelane_b32 v255, s0, 18
	s_add_i32 s0, s10, -16
	v_add_u32_e32 v117, 0x1ef00, v111
	v_add_u32_e32 v119, 0x16100, v111
	v_add_u32_e32 v120, 0x1d500, v111
	v_add_u32_e32 v121, 0x4800, v111
	v_add_u32_e32 v122, 0xd800, v111
	v_add_u32_e32 v123, 0x9000, v111
	v_add_u32_e32 v124, 0xfc00, v111
	v_add_u32_e32 v125, 0x16800, v111
	v_add_u32_e32 v126, 0x18c00, v111
	v_add_u32_e32 v127, 0x1b000, v111
	v_add_u32_e32 v128, 0x1dd00, v111
	v_add_u32_e32 v131, 0x14400, v130
	s_movk_i32 s75, 0xfc0
	v_lshl_add_u32 v135, v134, 9, v92
	v_add_u32_e32 v93, 0x200, v92
	v_writelane_b32 v255, s0, 19
	s_mov_b32 s24, -1
	v_lshlrev_b32_e32 v94, 2, v0
	v_readlane_b32 s73, v253, 43
	v_readlane_b32 s74, v253, 44
	v_readlane_b32 s76, v253, 46
	v_readlane_b32 s77, v253, 47
	v_readlane_b32 s78, v253, 48
	v_readlane_b32 s79, v253, 49
	v_readlane_b32 s86, v253, 56
	v_readlane_b32 s87, v253, 57
	v_and_b32_e32 v222, 15, v92
	v_lshrrev_b32_e32 v221, 4, v92
	v_readlane_b32 s1, v255, 18
	v_and_b32_e32 v221, 3, v221
	s_movk_i32 s0, 0x90
	v_lshlrev_b32_e32 v220, 4, v221
	v_lshlrev_b32_e32 v223, 2, v221
	v_mad_u32_u24 v220, v222, s0, v220
	v_lshl_add_u32 v221, v221, 3, v111
	v_add_u32_e32 v220, v220, v111
	v_mad_u32_u24 v221, v222, s0, v221
	v_sub_u32_e32 v222, v222, v223
	s_add_i32 s1, s1, 7
	s_cmp_gt_i32 s1, 2
	s_cselect_b32 s0, 1, 0
	s_sub_i32 s1, s1, s0
	s_lshr_b32 s0, s1, 4
	s_bfe_u32 s12, s1, 0x20002
	s_and_b32 s11, s1, 3
	s_mul_i32 s100, s12, 0x900
	s_mul_i32 s101, s11, 0x900
	s_lshl_b32 s10, s12, 5
	s_sub_i32 s11, s11, s12
	s_add_i32 s10, s10, s101
	s_lshl_b32 s11, s11, 4
	s_and_b32 s12, s0, 1
	s_mul_i32 s12, s12, 0x4800
	s_sub_i32 s100, s100, s12
	s_add_i32 s100, s100, 0x9000
	s_mul_i32 s12, s0, 0x2400
	s_add_i32 s10, s10, s12
	s_add_i32 s10, s10, 0x16800
	s_cmp_lg_u32 s0, 0
	s_cselect_b32 s12, 0xd800, 0
	s_addc_u32 s11, s11, 0
	s_add_i32 s101, s101, s12
	v_add_u32_e32 v190, s100, v220
	v_add_u32_e32 v200, s101, v220
	v_add_u32_e32 v208, s10, v221
	v_add_u32_e32 v233, s11, v222
	s_add_i32 s1, s1, 6
	s_lshr_b32 s0, s1, 4
	s_bfe_u32 s12, s1, 0x20002
	s_and_b32 s11, s1, 3
	s_mul_i32 s100, s12, 0x900
	s_mul_i32 s101, s11, 0x900
	s_lshl_b32 s10, s12, 5
	s_sub_i32 s11, s11, s12
	s_add_i32 s10, s10, s101
	s_lshl_b32 s11, s11, 4
	s_and_b32 s12, s0, 1
	s_mul_i32 s12, s12, 0x4800
	s_sub_i32 s100, s100, s12
	s_add_i32 s100, s100, 0x9000
	s_mul_i32 s12, s0, 0x2400
	s_add_i32 s10, s10, s12
	s_add_i32 s10, s10, 0x16800
	s_cmp_lg_u32 s0, 0
	s_cselect_b32 s12, 0xd800, 0
	s_addc_u32 s11, s11, 0
	s_add_i32 s101, s101, s12
	v_add_u32_e32 v191, s100, v220
	v_add_u32_e32 v201, s101, v220
	v_add_u32_e32 v209, s10, v221
	v_add_u32_e32 v234, s11, v222
	s_add_i32 s1, s1, 6
	s_lshr_b32 s0, s1, 4
	s_bfe_u32 s12, s1, 0x20002
	s_and_b32 s11, s1, 3
	s_mul_i32 s100, s12, 0x900
	s_mul_i32 s101, s11, 0x900
	s_lshl_b32 s10, s12, 5
	s_sub_i32 s11, s11, s12
	s_add_i32 s10, s10, s101
	s_lshl_b32 s11, s11, 4
	s_and_b32 s12, s0, 1
	s_mul_i32 s12, s12, 0x4800
	s_sub_i32 s100, s100, s12
	s_add_i32 s100, s100, 0x9000
	s_mul_i32 s12, s0, 0x2400
	s_add_i32 s10, s10, s12
	s_add_i32 s10, s10, 0x16800
	s_cmp_lg_u32 s0, 0
	s_cselect_b32 s12, 0xd800, 0
	s_addc_u32 s11, s11, 0
	s_add_i32 s101, s101, s12
	v_add_u32_e32 v192, s100, v220
	v_add_u32_e32 v202, s101, v220
	v_add_u32_e32 v210, s10, v221
	v_add_u32_e32 v235, s11, v222
	s_add_i32 s1, s1, 6
	s_lshr_b32 s0, s1, 4
	s_bfe_u32 s12, s1, 0x20002
	s_and_b32 s11, s1, 3
	s_mul_i32 s100, s12, 0x900
	s_mul_i32 s101, s11, 0x900
	s_lshl_b32 s10, s12, 5
	s_sub_i32 s11, s11, s12
	s_add_i32 s10, s10, s101
	s_lshl_b32 s11, s11, 4
	s_and_b32 s12, s0, 1
	s_mul_i32 s12, s12, 0x4800
	s_sub_i32 s100, s100, s12
	s_add_i32 s100, s100, 0x9000
	s_mul_i32 s12, s0, 0x2400
	s_add_i32 s10, s10, s12
	s_add_i32 s10, s10, 0x16800
	s_cmp_lg_u32 s0, 0
	s_cselect_b32 s12, 0xd800, 0
	s_addc_u32 s11, s11, 0
	s_add_i32 s101, s101, s12
	v_add_u32_e32 v193, s100, v220
	v_add_u32_e32 v203, s101, v220
	v_add_u32_e32 v211, s10, v221
	v_add_u32_e32 v236, s11, v222
	s_add_i32 s1, s1, 6
	s_lshr_b32 s0, s1, 4
	s_bfe_u32 s12, s1, 0x20002
	s_and_b32 s11, s1, 3
	s_mul_i32 s100, s12, 0x900
	s_mul_i32 s101, s11, 0x900
	s_lshl_b32 s10, s12, 5
	s_sub_i32 s11, s11, s12
	s_add_i32 s10, s10, s101
	s_lshl_b32 s11, s11, 4
	s_and_b32 s12, s0, 1
	s_mul_i32 s12, s12, 0x4800
	s_sub_i32 s100, s100, s12
	s_add_i32 s100, s100, 0x9000
	s_mul_i32 s12, s0, 0x2400
	s_add_i32 s10, s10, s12
	s_add_i32 s10, s10, 0x16800
	s_cmp_lg_u32 s0, 0
	s_cselect_b32 s12, 0xd800, 0
	s_addc_u32 s11, s11, 0
	s_add_i32 s101, s101, s12
	v_add_u32_e32 v194, s100, v220
	v_add_u32_e32 v204, s101, v220
	v_add_u32_e32 v229, s10, v221
	v_add_u32_e32 v237, s11, v222
	s_add_i32 s1, s1, 6
	s_lshr_b32 s0, s1, 4
	s_bfe_u32 s12, s1, 0x20002
	s_and_b32 s11, s1, 3
	s_mul_i32 s100, s12, 0x900
	s_mul_i32 s101, s11, 0x900
	s_lshl_b32 s10, s12, 5
	s_sub_i32 s11, s11, s12
	s_add_i32 s10, s10, s101
	s_lshl_b32 s11, s11, 4
	s_and_b32 s12, s0, 1
	s_mul_i32 s12, s12, 0x4800
	s_sub_i32 s100, s100, s12
	s_add_i32 s100, s100, 0x9000
	s_mul_i32 s12, s0, 0x2400
	s_add_i32 s10, s10, s12
	s_add_i32 s10, s10, 0x16800
	s_cmp_lg_u32 s0, 0
	s_cselect_b32 s12, 0xd800, 0
	s_addc_u32 s11, s11, 0
	s_add_i32 s101, s101, s12
	v_add_u32_e32 v195, s100, v220
	v_add_u32_e32 v205, s101, v220
	v_add_u32_e32 v230, s10, v221
	v_add_u32_e32 v238, s11, v222
	s_add_i32 s1, s1, 6
	s_lshr_b32 s0, s1, 4
	s_bfe_u32 s12, s1, 0x20002
	s_and_b32 s11, s1, 3
	s_mul_i32 s100, s12, 0x900
	s_mul_i32 s101, s11, 0x900
	s_lshl_b32 s10, s12, 5
	s_sub_i32 s11, s11, s12
	s_add_i32 s10, s10, s101
	s_lshl_b32 s11, s11, 4
	s_and_b32 s12, s0, 1
	s_mul_i32 s12, s12, 0x4800
	s_sub_i32 s100, s100, s12
	s_add_i32 s100, s100, 0x9000
	s_mul_i32 s12, s0, 0x2400
	s_add_i32 s10, s10, s12
	s_add_i32 s10, s10, 0x16800
	s_cmp_lg_u32 s0, 0
	s_cselect_b32 s12, 0xd800, 0
	s_addc_u32 s11, s11, 0
	s_add_i32 s101, s101, s12
	v_add_u32_e32 v196, s100, v220
	v_add_u32_e32 v206, s101, v220
	v_add_u32_e32 v231, s10, v221
	v_add_u32_e32 v239, s11, v222
	s_add_i32 s1, s1, 6
	s_lshr_b32 s0, s1, 4
	s_bfe_u32 s12, s1, 0x20002
	s_and_b32 s11, s1, 3
	s_mul_i32 s100, s12, 0x900
	s_mul_i32 s101, s11, 0x900
	s_lshl_b32 s10, s12, 5
	s_sub_i32 s11, s11, s12
	s_add_i32 s10, s10, s101
	s_lshl_b32 s11, s11, 4
	s_and_b32 s12, s0, 1
	s_mul_i32 s12, s12, 0x4800
	s_sub_i32 s100, s100, s12
	s_add_i32 s100, s100, 0x9000
	s_mul_i32 s12, s0, 0x2400
	s_add_i32 s10, s10, s12
	s_add_i32 s10, s10, 0x16800
	s_cmp_lg_u32 s0, 0
	s_cselect_b32 s12, 0xd800, 0
	s_addc_u32 s11, s11, 0
	s_add_i32 s101, s101, s12
	v_add_u32_e32 v197, s100, v220
	v_add_u32_e32 v207, s101, v220
	v_add_u32_e32 v232, s10, v221
	v_add_u32_e32 v240, s11, v222
	s_branch .LBB0_381

.LBB0_426:
	s_or_b64 exec, exec, s[0:1]
	v_or_b32_e32 v0, s62, v51
	v_mul_lo_u32 v0, v0, s39
	v_add3_u32 v4, v111, v0, v44
	s_waitcnt lgkmcnt(0)
	s_barrier
	ds_read_b128 v[6:9], v4 offset:18432
	v_or_b32_e32 v22, s64, v51
	v_mul_u32_u24_e32 v2, 0x90, v22
	v_add3_u32 v2, v111, v2, v44
	ds_read_b128 v[10:13], v2
	ds_read_b128 v[14:17], v4 offset:18496
	ds_read_b128 v[18:21], v2 offset:64
	s_waitcnt lgkmcnt(2)
	v_mfma_f32_16x16x32_bf16 v[6:9], v[6:9], v[10:13], 0
	v_or_b32_e32 v1, s62, v45
	v_or_b32_e32 v24, 2, v1
	v_or_b32_e32 v25, 3, v1
	v_or_b32_e32 v23, 1, v1
	v_cmp_gt_i32_e64 s[10:11], v22, v24
	s_waitcnt lgkmcnt(0)
	v_mfma_f32_16x16x32_bf16 v[6:9], v[14:17], v[18:21], v[6:9]
	v_cmp_gt_i32_e64 s[12:13], v22, v25
	v_cmp_gt_i32_e64 s[8:9], v22, v23
	s_or_b64 s[10:11], s[12:13], s[10:11]
	v_cmp_gt_i32_e32 vcc, v22, v1
	s_or_b64 s[8:9], s[10:11], s[8:9]
	s_or_b64 vcc, s[8:9], vcc
	v_lshl_add_u32 v5, v45, 1, v129
	s_nop 0
	v_cndmask_b32_e64 v3, 0, v9, s[12:13]
	v_cndmask_b32_e64 v8, 0, v8, s[10:11]
	v_cndmask_b32_e64 v2, 0, v7, s[8:9]
	v_cndmask_b32_e32 v6, 0, v6, vcc
	v_mad_u32_u24 v10, v22, s39, v5
	v_cvt_pk_bf16_f32 v2, v6, v2
	v_cvt_pk_bf16_f32 v3, v8, v3
	ds_write_b64 v10, v[2:3]
	ds_read_b128 v[6:9], v4 offset:18432
	v_mov_b32_e32 v2, 0x900
	v_mad_u32_u24 v2, v22, s39, v2
	v_add3_u32 v3, v111, v2, v44
	ds_read_b128 v[10:13], v3
	ds_read_b128 v[14:17], v4 offset:18496
	ds_read_b128 v[18:21], v3 offset:64
	s_waitcnt lgkmcnt(2)
	v_mfma_f32_16x16x32_bf16 v[6:9], v[6:9], v[10:13], 0
	v_or_b32_e32 v22, 16, v22
	v_cmp_gt_i32_e64 s[10:11], v22, v24
	v_cmp_gt_i32_e64 s[12:13], v22, v25
	s_waitcnt lgkmcnt(0)
	v_mfma_f32_16x16x32_bf16 v[6:9], v[14:17], v[18:21], v[6:9]
	v_cmp_gt_i32_e64 s[8:9], v22, v23
	s_or_b64 s[10:11], s[12:13], s[10:11]
	v_cmp_gt_i32_e32 vcc, v22, v1
	s_or_b64 s[8:9], s[10:11], s[8:9]
	s_or_b64 vcc, s[8:9], vcc
	v_add_u32_e32 v1, v5, v2
	s_nop 1
	v_cndmask_b32_e64 v3, 0, v9, s[12:13]
	v_cndmask_b32_e64 v5, 0, v8, s[10:11]
	v_cndmask_b32_e64 v2, 0, v7, s[8:9]
	v_cndmask_b32_e32 v6, 0, v6, vcc
	v_cvt_pk_bf16_f32 v2, v6, v2
	v_cvt_pk_bf16_f32 v3, v5, v3
	s_and_b64 vcc, exec, s[54:55]
	ds_write_b64 v1, v[2:3]
	s_waitcnt lgkmcnt(0)
	s_barrier
	s_cbranch_vccz .LBB0_449
	v_readlane_b32 s1, v255, 18
	s_cmp_eq_u32 s1, -4
	s_cbranch_scc1 .Lt1b_done
	ds_read_b128 v[6:9], v190
	ds_read_b128 v[10:13], v200
	ds_read_b128 v[14:17], v190 offset:64
	ds_read_b128 v[216:219], v200 offset:64
	s_waitcnt lgkmcnt(0)
	v_mfma_f32_16x16x32_bf16 v[220:223], v[6:9], v[10:13], 0
	v_mfma_f32_16x16x32_bf16 v[220:223], v[14:17], v[216:219], v[220:223]
	ds_read_b128 v[6:9], v191
	ds_read_b128 v[10:13], v201
	ds_read_b128 v[14:17], v191 offset:64
	ds_read_b128 v[216:219], v201 offset:64
	v_cmp_lt_i32_e32 vcc, 0, v233
	v_cmp_lt_i32_e64 s[8:9], 1, v233
	s_nop 1
	v_cndmask_b32_e32 v220, 0, v220, vcc
	v_cmp_lt_i32_e32 vcc, 2, v233
	v_cndmask_b32_e64 v221, 0, v221, s[8:9]
	v_cmp_lt_i32_e64 s[8:9], 3, v233
	s_nop 0
	v_cndmask_b32_e32 v222, 0, v222, vcc
	v_cvt_pk_bf16_f32 v224, v220, v221
	v_cndmask_b32_e64 v223, 0, v223, s[8:9]
	v_cvt_pk_bf16_f32 v225, v222, v223
	ds_write_b64 v208, v[224:225]
	s_waitcnt lgkmcnt(0)
	v_mfma_f32_16x16x32_bf16 v[220:223], v[6:9], v[10:13], 0
	v_mfma_f32_16x16x32_bf16 v[220:223], v[14:17], v[216:219], v[220:223]
	ds_read_b128 v[6:9], v192
	ds_read_b128 v[10:13], v202
	ds_read_b128 v[14:17], v192 offset:64
	ds_read_b128 v[216:219], v202 offset:64
	v_cmp_lt_i32_e32 vcc, 0, v234
	v_cmp_lt_i32_e64 s[8:9], 1, v234
	s_nop 1
	v_cndmask_b32_e32 v220, 0, v220, vcc
	v_cmp_lt_i32_e32 vcc, 2, v234
	v_cndmask_b32_e64 v221, 0, v221, s[8:9]
	v_cmp_lt_i32_e64 s[8:9], 3, v234
	s_nop 0
	v_cndmask_b32_e32 v222, 0, v222, vcc
	v_cvt_pk_bf16_f32 v224, v220, v221
	v_cndmask_b32_e64 v223, 0, v223, s[8:9]
	v_cvt_pk_bf16_f32 v225, v222, v223
	ds_write_b64 v209, v[224:225]
	s_waitcnt lgkmcnt(0)
	v_mfma_f32_16x16x32_bf16 v[220:223], v[6:9], v[10:13], 0
	v_mfma_f32_16x16x32_bf16 v[220:223], v[14:17], v[216:219], v[220:223]
	ds_read_b128 v[6:9], v193
	ds_read_b128 v[10:13], v203
	ds_read_b128 v[14:17], v193 offset:64
	ds_read_b128 v[216:219], v203 offset:64
	v_cmp_lt_i32_e32 vcc, 0, v235
	v_cmp_lt_i32_e64 s[8:9], 1, v235
	s_nop 1
	v_cndmask_b32_e32 v220, 0, v220, vcc
	v_cmp_lt_i32_e32 vcc, 2, v235
	v_cndmask_b32_e64 v221, 0, v221, s[8:9]
	v_cmp_lt_i32_e64 s[8:9], 3, v235
	s_nop 0
	v_cndmask_b32_e32 v222, 0, v222, vcc
	v_cvt_pk_bf16_f32 v224, v220, v221
	v_cndmask_b32_e64 v223, 0, v223, s[8:9]
	v_cvt_pk_bf16_f32 v225, v222, v223
	ds_write_b64 v210, v[224:225]
	s_waitcnt lgkmcnt(0)
	v_mfma_f32_16x16x32_bf16 v[220:223], v[6:9], v[10:13], 0
	v_mfma_f32_16x16x32_bf16 v[220:223], v[14:17], v[216:219], v[220:223]
	ds_read_b128 v[6:9], v194
	ds_read_b128 v[10:13], v204
	ds_read_b128 v[14:17], v194 offset:64
	ds_read_b128 v[216:219], v204 offset:64
	v_cmp_lt_i32_e32 vcc, 0, v236
	v_cmp_lt_i32_e64 s[8:9], 1, v236
	s_nop 1
	v_cndmask_b32_e32 v220, 0, v220, vcc
	v_cmp_lt_i32_e32 vcc, 2, v236
	v_cndmask_b32_e64 v221, 0, v221, s[8:9]
	v_cmp_lt_i32_e64 s[8:9], 3, v236
	s_nop 0
	v_cndmask_b32_e32 v222, 0, v222, vcc
	v_cvt_pk_bf16_f32 v224, v220, v221
	v_cndmask_b32_e64 v223, 0, v223, s[8:9]
	v_cvt_pk_bf16_f32 v225, v222, v223
	ds_write_b64 v211, v[224:225]
	s_waitcnt lgkmcnt(0)
	v_mfma_f32_16x16x32_bf16 v[220:223], v[6:9], v[10:13], 0
	v_mfma_f32_16x16x32_bf16 v[220:223], v[14:17], v[216:219], v[220:223]
	ds_read_b128 v[6:9], v195
	ds_read_b128 v[10:13], v205
	ds_read_b128 v[14:17], v195 offset:64
	ds_read_b128 v[216:219], v205 offset:64
	v_cmp_lt_i32_e32 vcc, 0, v237
	v_cmp_lt_i32_e64 s[8:9], 1, v237
	s_nop 1
	v_cndmask_b32_e32 v220, 0, v220, vcc
	v_cmp_lt_i32_e32 vcc, 2, v237
	v_cndmask_b32_e64 v221, 0, v221, s[8:9]
	v_cmp_lt_i32_e64 s[8:9], 3, v237
	s_nop 0
	v_cndmask_b32_e32 v222, 0, v222, vcc
	v_cvt_pk_bf16_f32 v224, v220, v221
	v_cndmask_b32_e64 v223, 0, v223, s[8:9]
	v_cvt_pk_bf16_f32 v225, v222, v223
	ds_write_b64 v229, v[224:225]
	s_waitcnt lgkmcnt(0)
	v_mfma_f32_16x16x32_bf16 v[220:223], v[6:9], v[10:13], 0
	v_mfma_f32_16x16x32_bf16 v[220:223], v[14:17], v[216:219], v[220:223]
	ds_read_b128 v[6:9], v196
	ds_read_b128 v[10:13], v206
	ds_read_b128 v[14:17], v196 offset:64
	ds_read_b128 v[216:219], v206 offset:64
	v_cmp_lt_i32_e32 vcc, 0, v238
	v_cmp_lt_i32_e64 s[8:9], 1, v238
	s_nop 1
	v_cndmask_b32_e32 v220, 0, v220, vcc
	v_cmp_lt_i32_e32 vcc, 2, v238
	v_cndmask_b32_e64 v221, 0, v221, s[8:9]
	v_cmp_lt_i32_e64 s[8:9], 3, v238
	s_nop 0
	v_cndmask_b32_e32 v222, 0, v222, vcc
	v_cvt_pk_bf16_f32 v224, v220, v221
	v_cndmask_b32_e64 v223, 0, v223, s[8:9]
	v_cvt_pk_bf16_f32 v225, v222, v223
	ds_write_b64 v230, v[224:225]
	s_waitcnt lgkmcnt(0)
	v_mfma_f32_16x16x32_bf16 v[220:223], v[6:9], v[10:13], 0
	v_mfma_f32_16x16x32_bf16 v[220:223], v[14:17], v[216:219], v[220:223]
	ds_read_b128 v[6:9], v197
	ds_read_b128 v[10:13], v207
	ds_read_b128 v[14:17], v197 offset:64
	ds_read_b128 v[216:219], v207 offset:64
	v_cmp_lt_i32_e32 vcc, 0, v239
	v_cmp_lt_i32_e64 s[8:9], 1, v239
	s_nop 1
	v_cndmask_b32_e32 v220, 0, v220, vcc
	v_cmp_lt_i32_e32 vcc, 2, v239
	v_cndmask_b32_e64 v221, 0, v221, s[8:9]
	v_cmp_lt_i32_e64 s[8:9], 3, v239
	s_nop 0
	v_cndmask_b32_e32 v222, 0, v222, vcc
	v_cvt_pk_bf16_f32 v224, v220, v221
	v_cndmask_b32_e64 v223, 0, v223, s[8:9]
	v_cvt_pk_bf16_f32 v225, v222, v223
	ds_write_b64 v231, v[224:225]
	s_waitcnt lgkmcnt(0)
	v_mfma_f32_16x16x32_bf16 v[220:223], v[6:9], v[10:13], 0
	v_mfma_f32_16x16x32_bf16 v[220:223], v[14:17], v[216:219], v[220:223]
	s_nop 3
	v_cmp_lt_i32_e32 vcc, 0, v240
	v_cmp_lt_i32_e64 s[8:9], 1, v240
	s_nop 1
	v_cndmask_b32_e32 v220, 0, v220, vcc
	v_cmp_lt_i32_e32 vcc, 2, v240
	v_cndmask_b32_e64 v221, 0, v221, s[8:9]
	v_cmp_lt_i32_e64 s[8:9], 3, v240
	s_nop 0
	v_cndmask_b32_e32 v222, 0, v222, vcc
	v_cvt_pk_bf16_f32 v224, v220, v221
	v_cndmask_b32_e64 v223, 0, v223, s[8:9]
	v_cvt_pk_bf16_f32 v225, v222, v223
	ds_write_b64 v232, v[224:225]
